# v5 + slow path warms L2 with its own code (s_getpc + 16 KiB of loads) before refine
# speedup vs baseline: 1.0187x; 1.0095x over previous
.Lrg_slow:
	s_getpc_b64 s[4:5]
	s_and_b32 s4, s4, -16
	v_lshlrev_b32_e32 v2, 4, v1
	global_load_dwordx4 v[100:103], v2, s[4:5] offset:0
	global_load_dwordx4 v[104:107], v2, s[4:5] offset:1024
	global_load_dwordx4 v[108:111], v2, s[4:5] offset:2048
	global_load_dwordx4 v[112:115], v2, s[4:5] offset:3072
	s_add_u32 s4, s4, 0x1000
	s_addc_u32 s5, s5, 0
	global_load_dwordx4 v[116:119], v2, s[4:5] offset:0
	global_load_dwordx4 v[120:123], v2, s[4:5] offset:1024
	global_load_dwordx4 v[124:127], v2, s[4:5] offset:2048
	global_load_dwordx4 v[128:131], v2, s[4:5] offset:3072
	s_add_u32 s4, s4, 0x1000
	s_addc_u32 s5, s5, 0
	global_load_dwordx4 v[100:103], v2, s[4:5] offset:0
	global_load_dwordx4 v[104:107], v2, s[4:5] offset:1024
	global_load_dwordx4 v[108:111], v2, s[4:5] offset:2048
	global_load_dwordx4 v[112:115], v2, s[4:5] offset:3072
	s_add_u32 s4, s4, 0x1000
	s_addc_u32 s5, s5, 0
	global_load_dwordx4 v[116:119], v2, s[4:5] offset:0
	global_load_dwordx4 v[120:123], v2, s[4:5] offset:1024
	global_load_dwordx4 v[124:127], v2, s[4:5] offset:2048
	global_load_dwordx4 v[128:131], v2, s[4:5] offset:3072
	s_add_u32 s4, s4, 0x1000
	s_addc_u32 s5, s5, 0
	s_load_dwordx2 s[4:5], s[0:1], 0x28
	v_and_b32_e32 v26, 63, v0
	s_bfe_u32 s3, s2, 0x30003
	v_cmp_gt_u32_e64 s[10:11], 64, v0
	s_waitcnt lgkmcnt(0)
	s_load_dword s33, s[4:5], 0x0
	s_and_saveexec_b64 s[6:7], s[10:11]
	s_cbranch_execz .LBB2_3
	s_load_dwordx2 s[4:5], s[0:1], 0x30
	v_lshlrev_b32_e32 v1, 5, v0
	v_lshl_or_b32 v1, s3, 11, v1
	s_waitcnt lgkmcnt(0)
	global_load_dwordx4 v[8:11], v1, s[4:5]
	global_load_dwordx4 v[2:5], v1, s[4:5] offset:16
	v_mov_b32_e32 v1, s33
	s_waitcnt vmcnt(1)
	v_mov_b32_e32 v6, v8
	s_waitcnt vmcnt(0)
	v_mov_b32_e32 v7, v2
	v_mov_b32_e32 v2, v9
	v_mov_b32_e32 v8, v10
	v_mov_b32_e32 v9, v4
	v_mov_b32_e32 v4, v11
	v_pk_add_f32 v[2:3], v[6:7], v[2:3]
	v_pk_add_f32 v[4:5], v[8:9], v[4:5]
	s_nop 0
	v_pk_add_f32 v[2:3], v[2:3], v[4:5]
	s_nop 0
	v_add_f32_e32 v2, v2, v3
	v_fmamk_f32 v1, v2, 0x3c800000, v1
	v_add_f32_e32 v2, 0xba03126f, v1
	v_readlane_b32 s5, v1, 1
	v_add_f32_e32 v3, 0x3a03126f, v1
	v_readlane_b32 s8, v1, 2
	v_cmp_ge_f32_e32 vcc, s5, v2
	v_readlane_b32 s12, v1, 4
	v_readlane_b32 s14, v1, 6
	v_cndmask_b32_e64 v4, 0, 1, vcc
	v_cmp_gt_f32_e32 vcc, s5, v3
	v_readlane_b32 s16, v1, 8
	v_readlane_b32 s18, v1, 10
	v_cndmask_b32_e64 v5, 0, 1, vcc
	v_cmp_ge_f32_e32 vcc, s8, v2
	v_readlane_b32 s20, v1, 12
	v_readlane_b32 s4, v1, 0
	v_cndmask_b32_e64 v6, 0, 1, vcc
	v_cmp_gt_f32_e32 vcc, s8, v3
	v_readlane_b32 s9, v1, 3
	v_readlane_b32 s13, v1, 5
	v_cndmask_b32_e64 v7, 0, 1, vcc
	v_cmp_ge_f32_e32 vcc, s12, v2
	v_readlane_b32 s15, v1, 7
	v_readlane_b32 s17, v1, 9
	v_cndmask_b32_e64 v8, 0, 1, vcc
	v_cmp_gt_f32_e32 vcc, s12, v3
	v_readlane_b32 s19, v1, 11
	v_readlane_b32 s21, v1, 13
	v_cndmask_b32_e64 v9, 0, 1, vcc
	v_cmp_ge_f32_e32 vcc, s14, v2
	s_nop 1
	v_cndmask_b32_e64 v10, 0, 1, vcc
	v_cmp_gt_f32_e32 vcc, s14, v3
	s_nop 1
	v_cndmask_b32_e64 v11, 0, 1, vcc
	v_cmp_ge_f32_e32 vcc, s16, v2
	s_nop 1
	v_cndmask_b32_e64 v12, 0, 1, vcc
	v_cmp_gt_f32_e32 vcc, s16, v3
	s_nop 1
	v_cndmask_b32_e64 v13, 0, 1, vcc
	v_cmp_ge_f32_e32 vcc, s18, v2
	s_nop 1
	v_cndmask_b32_e64 v14, 0, 1, vcc
	v_cmp_gt_f32_e32 vcc, s18, v3
	s_nop 1
	v_cndmask_b32_e64 v15, 0, 1, vcc
	v_cmp_ge_f32_e32 vcc, s20, v2
	s_nop 1
	v_cndmask_b32_e64 v16, 0, 1, vcc
	v_cmp_gt_f32_e32 vcc, s20, v3
	s_nop 1
	v_cndmask_b32_e64 v17, 0, 1, vcc
	v_cmp_ge_f32_e32 vcc, s4, v2
	s_nop 1
	v_addc_co_u32_e32 v4, vcc, 0, v4, vcc
	v_cmp_gt_f32_e32 vcc, s4, v3
	v_readlane_b32 s4, v1, 14
	s_nop 0
	v_addc_co_u32_e32 v5, vcc, 0, v5, vcc
	v_cmp_ge_f32_e32 vcc, s9, v2
	s_nop 1
	v_addc_co_u32_e32 v4, vcc, v4, v6, vcc
	v_cmp_gt_f32_e32 vcc, s9, v3
	s_nop 1
	v_addc_co_u32_e32 v5, vcc, v5, v7, vcc
	v_cmp_ge_f32_e32 vcc, s13, v2
	s_nop 1
	v_addc_co_u32_e32 v4, vcc, v4, v8, vcc
	v_cmp_gt_f32_e32 vcc, s13, v3
	s_nop 1
	v_addc_co_u32_e32 v5, vcc, v5, v9, vcc
	v_cmp_ge_f32_e32 vcc, s15, v2
	s_nop 1
	v_addc_co_u32_e32 v4, vcc, v4, v10, vcc
	v_cmp_gt_f32_e32 vcc, s15, v3
	s_nop 1
	v_addc_co_u32_e32 v5, vcc, v5, v11, vcc
	v_cmp_ge_f32_e32 vcc, s17, v2
	s_nop 1
	v_addc_co_u32_e32 v4, vcc, v4, v12, vcc
	v_cmp_gt_f32_e32 vcc, s17, v3
	s_nop 1
	v_addc_co_u32_e32 v5, vcc, v5, v13, vcc
	v_cmp_ge_f32_e32 vcc, s19, v2
	s_nop 1
	v_addc_co_u32_e32 v4, vcc, v4, v14, vcc
	v_cmp_gt_f32_e32 vcc, s19, v3
	s_nop 1
	v_addc_co_u32_e32 v5, vcc, v5, v15, vcc
	v_cmp_ge_f32_e32 vcc, s21, v2
	s_nop 1
	v_addc_co_u32_e32 v4, vcc, v4, v16, vcc
	v_cmp_gt_f32_e32 vcc, s21, v3
	s_nop 1
	v_addc_co_u32_e32 v5, vcc, v5, v17, vcc
	v_cmp_ge_f32_e32 vcc, s4, v2
	s_nop 1
	v_cndmask_b32_e64 v6, 0, 1, vcc
	v_cmp_gt_f32_e32 vcc, s4, v3
	v_readlane_b32 s4, v1, 15
	s_nop 0
	v_cndmask_b32_e64 v7, 0, 1, vcc
	v_cmp_ge_f32_e32 vcc, s4, v2
	s_nop 1
	v_addc_co_u32_e32 v4, vcc, v4, v6, vcc
	v_cmp_gt_f32_e32 vcc, s4, v3
	v_readlane_b32 s4, v1, 16
	s_nop 0
	v_addc_co_u32_e32 v5, vcc, v5, v7, vcc
	v_cmp_ge_f32_e32 vcc, s4, v2
	s_nop 1
	v_cndmask_b32_e64 v6, 0, 1, vcc
	v_cmp_gt_f32_e32 vcc, s4, v3
	v_readlane_b32 s4, v1, 17
	s_nop 0
	v_cndmask_b32_e64 v7, 0, 1, vcc
	v_cmp_ge_f32_e32 vcc, s4, v2
	s_nop 1
	v_addc_co_u32_e32 v4, vcc, v4, v6, vcc
	v_cmp_gt_f32_e32 vcc, s4, v3
	v_readlane_b32 s4, v1, 18
	s_nop 0
	v_addc_co_u32_e32 v5, vcc, v5, v7, vcc
	v_cmp_ge_f32_e32 vcc, s4, v2
	s_nop 1
	v_cndmask_b32_e64 v6, 0, 1, vcc
	v_cmp_gt_f32_e32 vcc, s4, v3
	v_readlane_b32 s4, v1, 19
	s_nop 0
	v_cndmask_b32_e64 v7, 0, 1, vcc
	v_cmp_ge_f32_e32 vcc, s4, v2
	s_nop 1
	v_addc_co_u32_e32 v4, vcc, v4, v6, vcc
	v_cmp_gt_f32_e32 vcc, s4, v3
	v_readlane_b32 s4, v1, 20
	s_nop 0
	v_addc_co_u32_e32 v5, vcc, v5, v7, vcc
	v_cmp_ge_f32_e32 vcc, s4, v2
	s_nop 1
	v_cndmask_b32_e64 v6, 0, 1, vcc
	v_cmp_gt_f32_e32 vcc, s4, v3
	v_readlane_b32 s4, v1, 21
	s_nop 0
	v_cndmask_b32_e64 v7, 0, 1, vcc
	v_cmp_ge_f32_e32 vcc, s4, v2
	s_nop 1
	v_addc_co_u32_e32 v4, vcc, v4, v6, vcc
	v_cmp_gt_f32_e32 vcc, s4, v3
	v_readlane_b32 s4, v1, 22
	s_nop 0
	v_addc_co_u32_e32 v5, vcc, v5, v7, vcc
	v_cmp_ge_f32_e32 vcc, s4, v2
	s_nop 1
	v_cndmask_b32_e64 v6, 0, 1, vcc
	v_cmp_gt_f32_e32 vcc, s4, v3
	v_readlane_b32 s4, v1, 23
	s_nop 0
	v_cndmask_b32_e64 v7, 0, 1, vcc
	v_cmp_ge_f32_e32 vcc, s4, v2
	s_nop 1
	v_addc_co_u32_e32 v4, vcc, v4, v6, vcc
	v_cmp_gt_f32_e32 vcc, s4, v3
	v_readlane_b32 s4, v1, 24
	s_nop 0
	v_addc_co_u32_e32 v5, vcc, v5, v7, vcc
	v_cmp_ge_f32_e32 vcc, s4, v2
	s_nop 1
	v_cndmask_b32_e64 v6, 0, 1, vcc
	v_cmp_gt_f32_e32 vcc, s4, v3
	v_readlane_b32 s4, v1, 25
	s_nop 0
	v_cndmask_b32_e64 v7, 0, 1, vcc
	v_cmp_ge_f32_e32 vcc, s4, v2
	s_nop 1
	v_addc_co_u32_e32 v4, vcc, v4, v6, vcc
	v_cmp_gt_f32_e32 vcc, s4, v3
	v_readlane_b32 s4, v1, 26
	s_nop 0
	v_addc_co_u32_e32 v5, vcc, v5, v7, vcc
	v_cmp_ge_f32_e32 vcc, s4, v2
	s_nop 1
	v_cndmask_b32_e64 v6, 0, 1, vcc
	v_cmp_gt_f32_e32 vcc, s4, v3
	v_readlane_b32 s4, v1, 27
	s_nop 0
	v_cndmask_b32_e64 v7, 0, 1, vcc
	v_cmp_ge_f32_e32 vcc, s4, v2
	s_nop 1
	v_addc_co_u32_e32 v4, vcc, v4, v6, vcc
	v_cmp_gt_f32_e32 vcc, s4, v3
	v_readlane_b32 s4, v1, 28
	s_nop 0
	v_addc_co_u32_e32 v5, vcc, v5, v7, vcc
	v_cmp_ge_f32_e32 vcc, s4, v2
	s_nop 1
	v_cndmask_b32_e64 v6, 0, 1, vcc
	v_cmp_gt_f32_e32 vcc, s4, v3
	v_readlane_b32 s4, v1, 29
	s_nop 0
	v_cndmask_b32_e64 v7, 0, 1, vcc
	v_cmp_ge_f32_e32 vcc, s4, v2
	s_nop 1
	v_addc_co_u32_e32 v4, vcc, v4, v6, vcc
	v_cmp_gt_f32_e32 vcc, s4, v3
	v_readlane_b32 s4, v1, 30
	s_nop 0
	v_addc_co_u32_e32 v5, vcc, v5, v7, vcc
	v_cmp_ge_f32_e32 vcc, s4, v2
	s_nop 1
	v_cndmask_b32_e64 v6, 0, 1, vcc
	v_cmp_gt_f32_e32 vcc, s4, v3
	v_readlane_b32 s4, v1, 31
	s_nop 0
	v_cndmask_b32_e64 v7, 0, 1, vcc
	v_cmp_ge_f32_e32 vcc, s4, v2
	s_nop 1
	v_addc_co_u32_e32 v4, vcc, v4, v6, vcc
	v_cmp_gt_f32_e32 vcc, s4, v3
	v_readlane_b32 s4, v1, 32
	s_nop 0
	v_addc_co_u32_e32 v5, vcc, v5, v7, vcc
	v_cmp_ge_f32_e32 vcc, s4, v2
	s_nop 1
	v_cndmask_b32_e64 v6, 0, 1, vcc
	v_cmp_gt_f32_e32 vcc, s4, v3
	v_readlane_b32 s4, v1, 33
	s_nop 0
	v_cndmask_b32_e64 v7, 0, 1, vcc
	v_cmp_ge_f32_e32 vcc, s4, v2
	s_nop 1
	v_addc_co_u32_e32 v4, vcc, v4, v6, vcc
	v_cmp_gt_f32_e32 vcc, s4, v3
	v_readlane_b32 s4, v1, 34
	s_nop 0
	v_addc_co_u32_e32 v5, vcc, v5, v7, vcc
	v_cmp_ge_f32_e32 vcc, s4, v2
	s_nop 1
	v_cndmask_b32_e64 v6, 0, 1, vcc
	v_cmp_gt_f32_e32 vcc, s4, v3
	v_readlane_b32 s4, v1, 35
	s_nop 0
	v_cndmask_b32_e64 v7, 0, 1, vcc
	v_cmp_ge_f32_e32 vcc, s4, v2
	s_nop 1
	v_addc_co_u32_e32 v4, vcc, v4, v6, vcc
	v_cmp_gt_f32_e32 vcc, s4, v3
	v_readlane_b32 s4, v1, 36
	s_nop 0
	v_addc_co_u32_e32 v5, vcc, v5, v7, vcc
	v_cmp_ge_f32_e32 vcc, s4, v2
	s_nop 1
	v_cndmask_b32_e64 v6, 0, 1, vcc
	v_cmp_gt_f32_e32 vcc, s4, v3
	v_readlane_b32 s4, v1, 37
	s_nop 0
	v_cndmask_b32_e64 v7, 0, 1, vcc
	v_cmp_ge_f32_e32 vcc, s4, v2
	s_nop 1
	v_addc_co_u32_e32 v4, vcc, v4, v6, vcc
	v_cmp_gt_f32_e32 vcc, s4, v3
	v_readlane_b32 s4, v1, 38
	s_nop 0
	v_addc_co_u32_e32 v5, vcc, v5, v7, vcc
	v_cmp_ge_f32_e32 vcc, s4, v2
	s_nop 1
	v_cndmask_b32_e64 v6, 0, 1, vcc
	v_cmp_gt_f32_e32 vcc, s4, v3
	v_readlane_b32 s4, v1, 39
	s_nop 0
	v_cndmask_b32_e64 v7, 0, 1, vcc
	v_cmp_ge_f32_e32 vcc, s4, v2
	s_nop 1
	v_addc_co_u32_e32 v4, vcc, v4, v6, vcc
	v_cmp_gt_f32_e32 vcc, s4, v3
	v_readlane_b32 s4, v1, 40
	s_nop 0
	v_addc_co_u32_e32 v5, vcc, v5, v7, vcc
	v_cmp_ge_f32_e32 vcc, s4, v2
	s_nop 1
	v_cndmask_b32_e64 v6, 0, 1, vcc
	v_cmp_gt_f32_e32 vcc, s4, v3
	v_readlane_b32 s4, v1, 41
	s_nop 0
	v_cndmask_b32_e64 v7, 0, 1, vcc
	v_cmp_ge_f32_e32 vcc, s4, v2
	s_nop 1
	v_addc_co_u32_e32 v4, vcc, v4, v6, vcc
	v_cmp_gt_f32_e32 vcc, s4, v3
	v_readlane_b32 s4, v1, 42
	s_nop 0
	v_addc_co_u32_e32 v5, vcc, v5, v7, vcc
	v_cmp_ge_f32_e32 vcc, s4, v2
	s_nop 1
	v_cndmask_b32_e64 v6, 0, 1, vcc
	v_cmp_gt_f32_e32 vcc, s4, v3
	v_readlane_b32 s4, v1, 43
	s_nop 0
	v_cndmask_b32_e64 v7, 0, 1, vcc
	v_cmp_ge_f32_e32 vcc, s4, v2
	s_nop 1
	v_addc_co_u32_e32 v4, vcc, v4, v6, vcc
	v_cmp_gt_f32_e32 vcc, s4, v3
	v_readlane_b32 s4, v1, 44
	s_nop 0
	v_addc_co_u32_e32 v5, vcc, v5, v7, vcc
	v_cmp_ge_f32_e32 vcc, s4, v2
	s_nop 1
	v_cndmask_b32_e64 v6, 0, 1, vcc
	v_cmp_gt_f32_e32 vcc, s4, v3
	v_readlane_b32 s4, v1, 45
	s_nop 0
	v_cndmask_b32_e64 v7, 0, 1, vcc
	v_cmp_ge_f32_e32 vcc, s4, v2
	s_nop 1
	v_addc_co_u32_e32 v4, vcc, v4, v6, vcc
	v_cmp_gt_f32_e32 vcc, s4, v3
	v_readlane_b32 s4, v1, 46
	s_nop 0
	v_addc_co_u32_e32 v5, vcc, v5, v7, vcc
	v_cmp_ge_f32_e32 vcc, s4, v2
	s_nop 1
	v_cndmask_b32_e64 v6, 0, 1, vcc
	v_cmp_gt_f32_e32 vcc, s4, v3
	v_readlane_b32 s4, v1, 47
	s_nop 0
	v_cndmask_b32_e64 v7, 0, 1, vcc
	v_cmp_ge_f32_e32 vcc, s4, v2
	s_nop 1
	v_addc_co_u32_e32 v4, vcc, v4, v6, vcc
	v_cmp_gt_f32_e32 vcc, s4, v3
	v_readlane_b32 s4, v1, 48
	s_nop 0
	v_addc_co_u32_e32 v5, vcc, v5, v7, vcc
	v_cmp_ge_f32_e32 vcc, s4, v2
	s_nop 1
	v_cndmask_b32_e64 v6, 0, 1, vcc
	v_cmp_gt_f32_e32 vcc, s4, v3
	v_readlane_b32 s4, v1, 49
	s_nop 0
	v_cndmask_b32_e64 v7, 0, 1, vcc
	v_cmp_ge_f32_e32 vcc, s4, v2
	s_nop 1
	v_addc_co_u32_e32 v4, vcc, v4, v6, vcc
	v_cmp_gt_f32_e32 vcc, s4, v3
	v_readlane_b32 s4, v1, 50
	s_nop 0
	v_addc_co_u32_e32 v5, vcc, v5, v7, vcc
	v_cmp_ge_f32_e32 vcc, s4, v2
	s_nop 1
	v_cndmask_b32_e64 v6, 0, 1, vcc
	v_cmp_gt_f32_e32 vcc, s4, v3
	v_readlane_b32 s4, v1, 51
	s_nop 0
	v_cndmask_b32_e64 v7, 0, 1, vcc
	v_cmp_ge_f32_e32 vcc, s4, v2
	s_nop 1
	v_addc_co_u32_e32 v4, vcc, v4, v6, vcc
	v_cmp_gt_f32_e32 vcc, s4, v3
	v_readlane_b32 s4, v1, 52
	s_nop 0
	v_addc_co_u32_e32 v5, vcc, v5, v7, vcc
	v_cmp_ge_f32_e32 vcc, s4, v2
	s_nop 1
	v_cndmask_b32_e64 v6, 0, 1, vcc
	v_cmp_gt_f32_e32 vcc, s4, v3
	v_readlane_b32 s4, v1, 53
	s_nop 0
	v_cndmask_b32_e64 v7, 0, 1, vcc
	v_cmp_ge_f32_e32 vcc, s4, v2
	s_nop 1
	v_addc_co_u32_e32 v4, vcc, v4, v6, vcc
	v_cmp_gt_f32_e32 vcc, s4, v3
	v_readlane_b32 s4, v1, 54
	s_nop 0
	v_addc_co_u32_e32 v5, vcc, v5, v7, vcc
	v_cmp_ge_f32_e32 vcc, s4, v2
	s_nop 1
	v_cndmask_b32_e64 v6, 0, 1, vcc
	v_cmp_gt_f32_e32 vcc, s4, v3
	v_readlane_b32 s4, v1, 55
	s_nop 0
	v_cndmask_b32_e64 v7, 0, 1, vcc
	v_cmp_ge_f32_e32 vcc, s4, v2
	s_nop 1
	v_addc_co_u32_e32 v4, vcc, v4, v6, vcc
	v_cmp_gt_f32_e32 vcc, s4, v3
	v_readlane_b32 s4, v1, 56
	s_nop 0
	v_addc_co_u32_e32 v5, vcc, v5, v7, vcc
	v_cmp_ge_f32_e32 vcc, s4, v2
	s_nop 1
	v_cndmask_b32_e64 v6, 0, 1, vcc
	v_cmp_gt_f32_e32 vcc, s4, v3
	v_readlane_b32 s4, v1, 57
	s_nop 0
	v_cndmask_b32_e64 v7, 0, 1, vcc
	v_cmp_ge_f32_e32 vcc, s4, v2
	s_nop 1
	v_addc_co_u32_e32 v4, vcc, v4, v6, vcc
	v_cmp_gt_f32_e32 vcc, s4, v3
	v_readlane_b32 s4, v1, 58
	s_nop 0
	v_addc_co_u32_e32 v5, vcc, v5, v7, vcc
	v_cmp_ge_f32_e32 vcc, s4, v2
	s_nop 1
	v_cndmask_b32_e64 v6, 0, 1, vcc
	v_cmp_gt_f32_e32 vcc, s4, v3
	v_readlane_b32 s4, v1, 59
	s_nop 0
	v_cndmask_b32_e64 v7, 0, 1, vcc
	v_cmp_ge_f32_e32 vcc, s4, v2
	s_nop 1
	v_addc_co_u32_e32 v4, vcc, v4, v6, vcc
	v_cmp_gt_f32_e32 vcc, s4, v3
	v_readlane_b32 s4, v1, 60
	s_nop 0
	v_addc_co_u32_e32 v5, vcc, v5, v7, vcc
	v_cmp_ge_f32_e32 vcc, s4, v2
	s_nop 1
	v_cndmask_b32_e64 v6, 0, 1, vcc
	v_cmp_gt_f32_e32 vcc, s4, v3
	v_readlane_b32 s4, v1, 61
	s_nop 0
	v_cndmask_b32_e64 v7, 0, 1, vcc
	v_cmp_ge_f32_e32 vcc, s4, v2
	s_nop 1
	v_addc_co_u32_e32 v4, vcc, v4, v6, vcc
	v_cmp_gt_f32_e32 vcc, s4, v3
	v_readlane_b32 s4, v1, 62
	s_nop 0
	v_addc_co_u32_e32 v5, vcc, v5, v7, vcc
	v_cmp_ge_f32_e32 vcc, s4, v2
	s_nop 1
	v_cndmask_b32_e64 v6, 0, 1, vcc
	v_cmp_gt_f32_e32 vcc, s4, v3
	v_readlane_b32 s4, v1, 63
	s_nop 0
	v_cndmask_b32_e64 v7, 0, 1, vcc
	v_cmp_ge_f32_e32 vcc, s4, v2
	s_nop 1
	v_addc_co_u32_e32 v1, vcc, v4, v6, vcc
	v_cmp_gt_f32_e32 vcc, s4, v3
	v_cmp_gt_u32_e64 s[8:9], 33, v1
	s_nop 0
	v_addc_co_u32_e32 v2, vcc, v5, v7, vcc
	v_cmp_lt_u32_e32 vcc, 32, v1
	v_cmp_gt_u32_e64 s[4:5], 32, v2
	s_and_b64 s[4:5], vcc, s[4:5]
	s_nop 0
	v_cndmask_b32_e64 v2, 0, 1, s[4:5]
	v_cmp_ne_u32_e32 vcc, 0, v2
	v_cmp_eq_u32_e64 s[4:5], 0, v26
	s_and_b64 exec, exec, s[4:5]
	s_cbranch_execz .LBB2_3
	v_mov_b32_e32 v2, s8
	v_mov_b32_e32 v3, s9
	v_mov_b32_e32 v4, vcc_lo
	v_mov_b32_e32 v5, vcc_hi
	v_mov_b32_e32 v1, 0
	ds_write_b128 v1, v[2:5] offset:16400
